# attention loop: second-step S accumulators start from the running-max initialiser directly (eight v_mov_b64 copies per iteration removed)
# baseline (speedup 1.0000x reference)
; template <bool FIRST>
; __device__ __forceinline__ bool partialSM(f32x16& p0, f32x16& p1, float& M, f32x16& minit, float& alpha) {
;     float tmax = p0[0]; for (int r = 1; r < 16; ++r) tmax = fmaxf(tmax, p0[r]); for (int r = 0; r < 16; ++r) tmax = fmaxf(tmax, p1[r]);
;     { auto rr = __builtin_amdgcn_permlane32_swap(__float_as_uint(tmax), __float_as_uint(tmax), false, false);
;       tmax = fmaxf(__uint_as_float(rr[0]), __uint_as_float(rr[1])); }
;     const float d0 = tmax - PLOG2;
;     const bool moved = FIRST || !__all(d0 <= THR * 1.4426950408889634f);
;     if (__builtin_expect(moved, FIRST)) {
;         const float d = FIRST ? d0 : fmaxf(d0, 0.f);
;         alpha = __builtin_amdgcn_exp2f(-d); M += d;
;         for (int r = 0; r < 16; ++r) { p0[r] -= d; p1[r] -= d; }
;         const float mi = PLOG2 - M;
;         for (int r = 0; r < 16; ++r) minit[r] = mi;
;     } else alpha = 1.f;
.LBB0_534:
	v_max_f32_e32 v96, v129, v129
	v_max_f32_e32 v97, v128, v128
	v_max_f32_e32 v96, v97, v96
	v_max3_f32 v96, v96, v130, v131
	v_max3_f32 v96, v96, v132, v133
	v_max3_f32 v96, v96, v134, v135
	v_max3_f32 v96, v96, v136, v137
	v_max3_f32 v96, v96, v138, v139
	v_max3_f32 v96, v96, v140, v141
	v_max3_f32 v96, v96, v142, v143
	v_max3_f32 v96, v96, v112, v113
	v_max3_f32 v96, v96, v114, v115
	v_max3_f32 v96, v96, v116, v117
	v_max3_f32 v96, v96, v118, v119
	v_max3_f32 v96, v96, v120, v121
	v_max3_f32 v96, v96, v122, v123
	v_max3_f32 v96, v96, v124, v125
	v_max3_f32 v96, v96, v126, v127
	v_mov_b32_e32 v97, v96
	s_nop 1
	v_permlane32_swap_b32_e32 v96, v97
	v_max_f32_e32 v97, v97, v97
	v_max_f32_e32 v96, v96, v96
	v_max_f32_e32 v96, v96, v97
	v_add_f32_e32 v96, -4.0, v96
	v_cmp_ge_f32_e32 vcc, s30, v96
	s_cmp_lg_u64 vcc, exec
	s_cselect_b64 s[90:91], -1, 0
	s_cmp_eq_u64 vcc, exec
	s_cbranch_scc0 .LBB0_545
	v_mov_b32_e32 v201, 1.0
	s_andn2_b64 vcc, exec, s[90:91]
	s_cbranch_vccnz .LBB0_539

; __device__ __forceinline__ unsigned cvt_pk4_fp8(float a, float b, float c, float d) { int w; asm("" : "=v"(w));     w = __builtin_amdgcn_cvt_pk_fp8_f32(a, b, w, false); w = __builtin_amdgcn_cvt_pk_fp8_f32(c, d, w, true); return (unsigned)w; }
; __device__ __forceinline__ void finishSM(f32x16& p0, f32x16& p1, i32x8& pa) {
;     for (int r = 0; r < 16; ++r) p1[r] = __builtin_amdgcn_exp2f(p1[r]);
; #pragma unroll
;     for (int v = 0; v < 4; ++v) { pa[v] = (int)cvt_pk4_fp8(p0[4 * v], p0[4 * v + 1], p0[4 * v + 2], p0[4 * v + 3]); pa[4 + v] = (int)cvt_pk4_fp8(p1[4 * v], p1[4 * v + 1], p1[4 * v + 2], p1[4 * v + 3]); }
; }
; __device__ __forceinline__ void qkt(f32x16& p0, f32x16& p1, const char* stg, int ka, const i32x8* qf, const f32x16& minit) {
;     p0 = minit; p1 = minit;
; #pragma unroll
;     for (int s = 0; s < 3; ++s) { const char* a = stg + SOFF_K + s * 4096 + ka; const char* b = stg + SOFF_K + s * 4096 + (ka ^ 16);
;         const i32x4 a0 = *reinterpret_cast<const i32x4*>(a), a1 = *reinterpret_cast<const i32x4*>(b);
;         const i32x4 c0 = *reinterpret_cast<const i32x4*>(a + 2048), c1 = *reinterpret_cast<const i32x4*>(b + 2048);
;         p0 = __builtin_amdgcn_mfma_scale_f32_32x32x64_f8f6f4(__builtin_shufflevector(a0, a1, 0, 1, 2, 3, 4, 5, 6, 7), qf[s], p0, 0, 0, 0, 0, 0, 0);
;         p1 = __builtin_amdgcn_mfma_scale_f32_32x32x64_f8f6f4(__builtin_shufflevector(c0, c1, 0, 1, 2, 3, 4, 5, 6, 7), qf[s], p1, 0, 0, 0, 0, 0, 0); }
; }
; __device__ __forceinline__ void v_read(i32x8 (&vf)[4], const char* stg, int ka) {
; #pragma unroll
;     for (int d0 = 0; d0 < 4; ++d0) { const i32x4 a0 = *reinterpret_cast<const i32x4*>(stg + SOFF_V + d0 * 2048 + ka), a1 = *reinterpret_cast<const i32x4*>(stg + SOFF_V + d0 * 2048 + (ka ^ 16));
;         vf[d0] = __builtin_shufflevector(a0, a1, 0, 1, 2, 3, 4, 5, 6, 7); }
; }
; __device__ __forceinline__ void pv_mma(f32x16* o, f32x16& ol, const i32x8 (&vf)[4], const i32x8 ones, const i32x8 pa) {
; #pragma unroll
;     for (int d0 = 0; d0 < 4; ++d0) o[d0] = __builtin_amdgcn_mfma_scale_f32_32x32x64_f8f6f4(pa, vf[d0], o[d0], 0, 0, 0, 0, 0, 0);
;     ol = __builtin_amdgcn_mfma_scale_f32_32x32x64_f8f6f4(pa, ones, ol, 0, 0, 0, 0, 0, 0);
; }
.LBB0_539:
	s_cmp_gt_i32 s1, 3
	s_cselect_b32 s46, -4, 2
	s_add_i32 s1, s46, s1
	v_exp_f32_e32 v201, v128
	v_exp_f32_e32 v218, v129
	v_exp_f32_e32 v219, v130
	v_exp_f32_e32 v220, v131
	v_exp_f32_e32 v221, v132
	v_exp_f32_e32 v222, v133
	v_exp_f32_e32 v223, v134
	v_exp_f32_e32 v224, v135
	v_exp_f32_e32 v225, v136
	v_exp_f32_e32 v226, v137
	v_exp_f32_e32 v227, v138
	v_exp_f32_e32 v228, v139
	v_exp_f32_e32 v229, v140
	v_exp_f32_e32 v230, v141
	v_exp_f32_e32 v231, v142
	v_exp_f32_e32 v232, v143
	s_mul_i32 s92, s1, 0x5000
	s_add_i32 s46, s92, 0
	v_add_u32_e32 v233, s46, v193
	v_add_u32_e32 v234, s46, v194
	ds_read_b128 v[202:205], v233
	ds_read_b128 v[206:209], v234
	ds_read_b128 v[210:213], v233 offset:2048
	ds_read_b128 v[214:217], v234 offset:2048
	ds_read_b128 v[236:239], v233 offset:4096
	ds_read_b128 v[240:243], v234 offset:4096
	ds_read_b128 v[244:247], v233 offset:6144
	ds_read_b128 v[248:251], v234 offset:6144
	v_exp_f32_e32 v113, v113
	s_waitcnt lgkmcnt(6)
	v_mfma_f32_32x32x64_f8f6f4 v[128:143], v[202:209], v[168:175], v[80:95]
	v_exp_f32_e32 v114, v114
	v_exp_f32_e32 v115, v115
	v_exp_f32_e32 v118, v118
	v_exp_f32_e32 v120, v120
	v_exp_f32_e32 v121, v121
	v_exp_f32_e32 v124, v124
	v_exp_f32_e32 v125, v125
	v_exp_f32_e32 v122, v122
	v_exp_f32_e32 v123, v123
	v_exp_f32_e32 v126, v126
	v_exp_f32_e32 v127, v127
	s_waitcnt lgkmcnt(4)
	v_mfma_f32_32x32x64_f8f6f4 v[96:111], v[210:217], v[168:175], v[80:95]
	ds_read_b128 v[202:205], v233 offset:8192
	ds_read_b128 v[206:209], v234 offset:8192
	ds_read_b128 v[210:213], v233 offset:10240
	ds_read_b128 v[214:217], v234 offset:10240
	s_waitcnt lgkmcnt(6)
	v_mfma_f32_32x32x64_f8f6f4 v[128:143], v[236:243], v[176:183], v[128:143]
	s_waitcnt lgkmcnt(4)
	v_mfma_f32_32x32x64_f8f6f4 v[96:111], v[244:251], v[176:183], v[96:111]
	ds_read_b128 v[240:243], v200 offset:12288
	ds_read_b128 v[236:239], v199 offset:12288
	ds_read_b128 v[244:247], v199 offset:14336
	ds_read_b128 v[248:251], v200 offset:14336
	s_waitcnt lgkmcnt(6)
	v_mfma_f32_32x32x64_f8f6f4 v[128:143], v[202:209], v[160:167], v[128:143]
	v_exp_f32_e32 v202, v112
	v_exp_f32_e32 v203, v116
	v_exp_f32_e32 v204, v117
	v_exp_f32_e32 v205, v119
	s_nop 0
	v_cvt_pk_fp8_f32 v116, v202, v113
	v_cvt_pk_fp8_f32 v117, v203, v204
	v_cvt_pk_fp8_f32 v116, v114, v115 op_sel:[0,0,1]
	v_cvt_pk_fp8_f32 v117, v118, v205 op_sel:[0,0,1]
	s_waitcnt lgkmcnt(4)
	v_mfma_f32_32x32x64_f8f6f4 v[96:111], v[210:217], v[160:167], v[96:111]
	v_cvt_pk_fp8_f32 v112, v201, v218
	v_cvt_pk_fp8_f32 v113, v221, v222
	v_cvt_pk_fp8_f32 v114, v225, v226
	v_cvt_pk_fp8_f32 v118, v120, v121
	v_cvt_pk_fp8_f32 v115, v229, v230
	v_cvt_pk_fp8_f32 v119, v124, v125
	v_cvt_pk_fp8_f32 v112, v219, v220 op_sel:[0,0,1]
	v_cvt_pk_fp8_f32 v113, v223, v224 op_sel:[0,0,1]
	v_cvt_pk_fp8_f32 v114, v227, v228 op_sel:[0,0,1]
	v_cvt_pk_fp8_f32 v118, v122, v123 op_sel:[0,0,1]
	v_cvt_pk_fp8_f32 v115, v231, v232 op_sel:[0,0,1]
	v_cvt_pk_fp8_f32 v119, v126, v127 op_sel:[0,0,1]
	ds_read_b128 v[124:127], v200 offset:16384
	ds_read_b128 v[120:123], v199 offset:16384
	v_mfma_f32_32x32x64_f8f6f4 v[64:79], v[112:119], v[152:159], v[64:79]
	s_cmp_le_i32 s38, s0
	s_waitcnt lgkmcnt(4)
	v_mfma_f32_32x32x64_f8f6f4 v[48:63], v[112:119], v[236:243], v[48:63]
	ds_read_b128 v[236:239], v199 offset:18432
	ds_read_b128 v[240:243], v200 offset:18432
	s_waitcnt lgkmcnt(4)
	v_mfma_f32_32x32x64_f8f6f4 v[32:47], v[112:119], v[244:251], v[32:47]
	s_waitcnt lgkmcnt(2)
	v_mfma_f32_32x32x64_f8f6f4 v[16:31], v[112:119], v[120:127], v[16:31]
	s_waitcnt lgkmcnt(0)
	v_mfma_f32_32x32x64_f8f6f4 v[0:15], v[112:119], v[236:243], v[0:15]
	s_cbranch_scc1 .LBB0_541
; __device__ __forceinline__ void mask_tile(f32x16& p0, f32x16& p1, int dq, unsigned W) {
;     const float NEG = -__builtin_inff();
; #pragma unroll
;     for (int r = 0; r < 16; ++r) {
;         const int c = (r & 3) + 8 * (r >> 2);
;         if ((unsigned)(dq - c) >= W) p0[r] = NEG;
;         if ((unsigned)(dq - c - 32) >= W) p1[r] = NEG;
;     }
; }
	v_add_u32_e32 v112, 0x4000003b, v196
	v_cmp_gt_u32_e32 vcc, 2.0, v112
	v_add_u32_e32 v112, 27, v196
	s_nop 0
	v_cndmask_b32_e32 v128, v187, v128, vcc
	v_cmp_lt_u32_e32 vcc, s3, v112
	v_add_u32_e32 v112, 58, v196
	s_nop 0
	v_cndmask_b32_e32 v96, v187, v96, vcc
	v_cmp_lt_u32_e32 vcc, s3, v112
	v_add_u32_e32 v112, 26, v196
	s_nop 0
	v_cndmask_b32_e32 v129, v187, v129, vcc
	v_cmp_lt_u32_e32 vcc, s3, v112
	v_add_u32_e32 v112, 57, v196
	s_nop 0
	v_cndmask_b32_e32 v97, v187, v97, vcc
	v_cmp_lt_u32_e32 vcc, s3, v112
	v_add_u32_e32 v112, 25, v196
	s_nop 0
	v_cndmask_b32_e32 v130, v187, v130, vcc
	v_cmp_lt_u32_e32 vcc, s3, v112
	v_add_u32_e32 v112, 56, v196
	s_nop 0
	v_cndmask_b32_e32 v98, v187, v98, vcc
	v_cmp_lt_u32_e32 vcc, s3, v112
	v_add_u32_e32 v112, 24, v196
	s_nop 0
	v_cndmask_b32_e32 v131, v187, v131, vcc
	v_cmp_lt_u32_e32 vcc, s3, v112
	v_add_u32_e32 v112, 51, v196
	s_nop 0
	v_cndmask_b32_e32 v99, v187, v99, vcc
	v_cmp_lt_u32_e32 vcc, s3, v112
	v_add_u32_e32 v112, 19, v196
	s_nop 0
	v_cndmask_b32_e32 v132, v187, v132, vcc
	v_cmp_lt_u32_e32 vcc, s3, v112
	v_add_u32_e32 v112, 50, v196
	s_nop 0
	v_cndmask_b32_e32 v100, v187, v100, vcc
	v_cmp_lt_u32_e32 vcc, s3, v112
	v_add_u32_e32 v112, 18, v196
	s_nop 0
	v_cndmask_b32_e32 v133, v187, v133, vcc
	v_cmp_lt_u32_e32 vcc, s3, v112
	v_add_u32_e32 v112, 49, v196
	s_nop 0
	v_cndmask_b32_e32 v101, v187, v101, vcc
	v_cmp_lt_u32_e32 vcc, s3, v112
	v_add_u32_e32 v112, 17, v196
	s_nop 0
	v_cndmask_b32_e32 v134, v187, v134, vcc
	v_cmp_lt_u32_e32 vcc, s3, v112
	v_add_u32_e32 v112, 48, v196
	s_nop 0
	v_cndmask_b32_e32 v102, v187, v102, vcc
	v_cmp_lt_u32_e32 vcc, s3, v112
	v_add_u32_e32 v112, 16, v196
	s_nop 0
	v_cndmask_b32_e32 v135, v187, v135, vcc
	v_cmp_lt_u32_e32 vcc, s3, v112
	v_add_u32_e32 v112, 43, v196
	s_nop 0
	v_cndmask_b32_e32 v103, v187, v103, vcc
	v_cmp_lt_u32_e32 vcc, s3, v112
	v_add_u32_e32 v112, 11, v196
	s_nop 0
	v_cndmask_b32_e32 v136, v187, v136, vcc
	v_cmp_lt_u32_e32 vcc, s3, v112
	v_add_u32_e32 v112, 42, v196
	s_nop 0
	v_cndmask_b32_e32 v104, v187, v104, vcc
	v_cmp_lt_u32_e32 vcc, s3, v112
	v_add_u32_e32 v112, 10, v196
	s_nop 0
	v_cndmask_b32_e32 v137, v187, v137, vcc
	v_cmp_lt_u32_e32 vcc, s3, v112
	v_add_u32_e32 v112, 41, v196
	s_nop 0
	v_cndmask_b32_e32 v105, v187, v105, vcc
	v_cmp_lt_u32_e32 vcc, s3, v112
	v_add_u32_e32 v112, 9, v196
	s_nop 0
	v_cndmask_b32_e32 v138, v187, v138, vcc
	v_cmp_lt_u32_e32 vcc, s3, v112
	v_add_u32_e32 v112, 40, v196
	s_nop 0
	v_cndmask_b32_e32 v106, v187, v106, vcc
	v_cmp_lt_u32_e32 vcc, s3, v112
	v_add_u32_e32 v112, 8, v196
	s_nop 0
	v_cndmask_b32_e32 v139, v187, v139, vcc
	v_cmp_lt_u32_e32 vcc, s3, v112
	v_add_u32_e32 v112, 35, v196
	s_nop 0
	v_cndmask_b32_e32 v107, v187, v107, vcc
	v_cmp_lt_u32_e32 vcc, s3, v112
	v_add_u32_e32 v112, 3, v196
	s_nop 0
	v_cndmask_b32_e32 v140, v187, v140, vcc
	v_cmp_lt_u32_e32 vcc, s3, v112
	v_add_u32_e32 v112, 34, v196
	s_nop 0
	v_cndmask_b32_e32 v108, v187, v108, vcc
	v_cmp_lt_u32_e32 vcc, s3, v112
	v_add_u32_e32 v112, 2, v196
	s_nop 0
	v_cndmask_b32_e32 v141, v187, v141, vcc
	v_cmp_lt_u32_e32 vcc, s3, v112
	v_add_u32_e32 v112, 33, v196
	s_nop 0
	v_cndmask_b32_e32 v109, v187, v109, vcc
	v_cmp_lt_u32_e32 vcc, s3, v112
	v_add_u32_e32 v112, 1, v196
	s_nop 0
	v_cndmask_b32_e32 v142, v187, v142, vcc
	v_cmp_lt_u32_e32 vcc, s3, v112
	v_add_u32_e32 v112, 32, v196
	s_nop 0
	v_cndmask_b32_e32 v110, v187, v110, vcc
	v_cmp_lt_u32_e32 vcc, s3, v112
	s_nop 1
	v_cndmask_b32_e32 v143, v187, v143, vcc
	v_cmp_lt_u32_e32 vcc, s3, v196
	s_nop 1
	v_cndmask_b32_e32 v111, v187, v111, vcc

; template <bool FIRST>
; __device__ __forceinline__ bool partialSM(f32x16& p0, f32x16& p1, float& M, f32x16& minit, float& alpha) {
;     float tmax = p0[0]; for (int r = 1; r < 16; ++r) tmax = fmaxf(tmax, p0[r]); for (int r = 0; r < 16; ++r) tmax = fmaxf(tmax, p1[r]);
;     { auto rr = __builtin_amdgcn_permlane32_swap(__float_as_uint(tmax), __float_as_uint(tmax), false, false);
;       tmax = fmaxf(__uint_as_float(rr[0]), __uint_as_float(rr[1])); }
;     const float d0 = tmax - PLOG2;
;     const bool moved = FIRST || !__all(d0 <= THR * 1.4426950408889634f);
;     if (__builtin_expect(moved, FIRST)) {
;         const float d = FIRST ? d0 : fmaxf(d0, 0.f);
;         alpha = __builtin_amdgcn_exp2f(-d); M += d;
;         for (int r = 0; r < 16; ++r) { p0[r] -= d; p1[r] -= d; }
;         const float mi = PLOG2 - M;
;         for (int r = 0; r < 16; ++r) minit[r] = mi;
;     } else alpha = 1.f;
.LBB0_596:
	v_max_f32_e32 v96, v129, v129
	v_max_f32_e32 v97, v128, v128
	v_max_f32_e32 v96, v97, v96
	v_max3_f32 v96, v96, v130, v131
	v_max3_f32 v96, v96, v132, v133
	v_max3_f32 v96, v96, v134, v135
	v_max3_f32 v96, v96, v136, v137
	v_max3_f32 v96, v96, v138, v139
	v_max3_f32 v96, v96, v140, v141
	v_max3_f32 v96, v96, v142, v143
	v_max3_f32 v96, v96, v112, v113
	v_max3_f32 v96, v96, v114, v115
	v_max3_f32 v96, v96, v116, v117
	v_max3_f32 v96, v96, v118, v119
	v_max3_f32 v96, v96, v120, v121
	v_max3_f32 v96, v96, v122, v123
	v_max3_f32 v96, v96, v124, v125
	v_max3_f32 v96, v96, v126, v127
	v_mov_b32_e32 v97, v96
	s_nop 1
	v_permlane32_swap_b32_e32 v96, v97
	v_max_f32_e32 v97, v97, v97
	v_max_f32_e32 v96, v96, v96
	v_max_f32_e32 v96, v96, v97
	v_add_f32_e32 v96, -4.0, v96
	v_cmp_ge_f32_e32 vcc, s31, v96
	s_cmp_lg_u64 vcc, exec
	s_cselect_b64 s[92:93], -1, 0
	s_cmp_eq_u64 vcc, exec
	s_cbranch_scc0 .LBB0_610
	v_mov_b32_e32 v201, 1.0
	s_andn2_b64 vcc, exec, s[92:93]
	s_cbranch_vccnz .LBB0_601

; __device__ __forceinline__ unsigned cvt_pk4_fp8(float a, float b, float c, float d) { int w; asm("" : "=v"(w));     w = __builtin_amdgcn_cvt_pk_fp8_f32(a, b, w, false); w = __builtin_amdgcn_cvt_pk_fp8_f32(c, d, w, true); return (unsigned)w; }
; __device__ __forceinline__ void finishSM(f32x16& p0, f32x16& p1, i32x8& pa) {
;     for (int r = 0; r < 16; ++r) p1[r] = __builtin_amdgcn_exp2f(p1[r]);
; #pragma unroll
;     for (int v = 0; v < 4; ++v) { pa[v] = (int)cvt_pk4_fp8(p0[4 * v], p0[4 * v + 1], p0[4 * v + 2], p0[4 * v + 3]); pa[4 + v] = (int)cvt_pk4_fp8(p1[4 * v], p1[4 * v + 1], p1[4 * v + 2], p1[4 * v + 3]); }
; }
; __device__ __forceinline__ void qkt(f32x16& p0, f32x16& p1, const char* stg, int ka, const i32x8* qf, const f32x16& minit) {
;     p0 = minit; p1 = minit;
; #pragma unroll
;     for (int s = 0; s < 3; ++s) { const char* a = stg + SOFF_K + s * 4096 + ka; const char* b = stg + SOFF_K + s * 4096 + (ka ^ 16);
;         const i32x4 a0 = *reinterpret_cast<const i32x4*>(a), a1 = *reinterpret_cast<const i32x4*>(b);
;         const i32x4 c0 = *reinterpret_cast<const i32x4*>(a + 2048), c1 = *reinterpret_cast<const i32x4*>(b + 2048);
;         p0 = __builtin_amdgcn_mfma_scale_f32_32x32x64_f8f6f4(__builtin_shufflevector(a0, a1, 0, 1, 2, 3, 4, 5, 6, 7), qf[s], p0, 0, 0, 0, 0, 0, 0);
;         p1 = __builtin_amdgcn_mfma_scale_f32_32x32x64_f8f6f4(__builtin_shufflevector(c0, c1, 0, 1, 2, 3, 4, 5, 6, 7), qf[s], p1, 0, 0, 0, 0, 0, 0); }
; }
; __device__ __forceinline__ void v_read(i32x8 (&vf)[4], const char* stg, int ka) {
; #pragma unroll
;     for (int d0 = 0; d0 < 4; ++d0) { const i32x4 a0 = *reinterpret_cast<const i32x4*>(stg + SOFF_V + d0 * 2048 + ka), a1 = *reinterpret_cast<const i32x4*>(stg + SOFF_V + d0 * 2048 + (ka ^ 16));
;         vf[d0] = __builtin_shufflevector(a0, a1, 0, 1, 2, 3, 4, 5, 6, 7); }
; }
; __device__ __forceinline__ void pv_mma(f32x16* o, f32x16& ol, const i32x8 (&vf)[4], const i32x8 ones, const i32x8 pa) {
; #pragma unroll
;     for (int d0 = 0; d0 < 4; ++d0) o[d0] = __builtin_amdgcn_mfma_scale_f32_32x32x64_f8f6f4(pa, vf[d0], o[d0], 0, 0, 0, 0, 0, 0);
;     ol = __builtin_amdgcn_mfma_scale_f32_32x32x64_f8f6f4(pa, ones, ol, 0, 0, 0, 0, 0, 0);
; }
.LBB0_601:
	s_cmp_gt_i32 s0, 3
	s_cselect_b32 s46, -4, 2
	s_add_i32 s0, s46, s0
	v_exp_f32_e32 v203, v128
	v_exp_f32_e32 v220, v129
	v_exp_f32_e32 v221, v130
	v_exp_f32_e32 v222, v131
	v_exp_f32_e32 v223, v132
	v_exp_f32_e32 v224, v133
	v_exp_f32_e32 v225, v134
	v_exp_f32_e32 v226, v135
	v_exp_f32_e32 v227, v136
	v_exp_f32_e32 v228, v137
	v_exp_f32_e32 v229, v138
	v_exp_f32_e32 v230, v139
	v_exp_f32_e32 v231, v140
	v_exp_f32_e32 v232, v141
	v_exp_f32_e32 v233, v142
	v_exp_f32_e32 v234, v143
	s_mul_i32 s46, s0, 0x5000
	s_add_i32 s46, s46, 0
	v_add_u32_e32 v202, s46, v192
	v_add_u32_e32 v201, s46, v193
	ds_read_b128 v[204:207], v202
	ds_read_b128 v[208:211], v201
	ds_read_b128 v[212:215], v202 offset:2048
	ds_read_b128 v[216:219], v201 offset:2048
	ds_read_b128 v[236:239], v202 offset:4096
	ds_read_b128 v[240:243], v201 offset:4096
	ds_read_b128 v[244:247], v202 offset:6144
	ds_read_b128 v[248:251], v201 offset:6144
	v_exp_f32_e32 v113, v113
	s_waitcnt lgkmcnt(6)
	v_mfma_f32_32x32x64_f8f6f4 v[128:143], v[204:211], v[168:175], v[80:95]
	v_exp_f32_e32 v114, v114
	v_exp_f32_e32 v115, v115
	v_exp_f32_e32 v118, v118
	v_exp_f32_e32 v120, v120
	v_exp_f32_e32 v121, v121
	v_exp_f32_e32 v124, v124
	v_exp_f32_e32 v125, v125
	v_exp_f32_e32 v122, v122
	v_exp_f32_e32 v123, v123
	v_exp_f32_e32 v126, v126
	v_exp_f32_e32 v127, v127
	s_waitcnt lgkmcnt(4)
	v_mfma_f32_32x32x64_f8f6f4 v[96:111], v[212:219], v[168:175], v[80:95]
	ds_read_b128 v[204:207], v202 offset:8192
	ds_read_b128 v[208:211], v201 offset:8192
	ds_read_b128 v[212:215], v202 offset:10240
	ds_read_b128 v[216:219], v201 offset:10240
	s_waitcnt lgkmcnt(6)
	v_mfma_f32_32x32x64_f8f6f4 v[128:143], v[236:243], v[176:183], v[128:143]
	s_waitcnt lgkmcnt(4)
	v_mfma_f32_32x32x64_f8f6f4 v[96:111], v[244:251], v[176:183], v[96:111]
	ds_read_b128 v[240:243], v200 offset:12288
	ds_read_b128 v[236:239], v199 offset:12288
	ds_read_b128 v[244:247], v199 offset:14336
	ds_read_b128 v[248:251], v200 offset:14336
	s_waitcnt lgkmcnt(6)
	v_mfma_f32_32x32x64_f8f6f4 v[128:143], v[204:211], v[160:167], v[128:143]
	v_exp_f32_e32 v204, v112
	v_exp_f32_e32 v205, v116
	v_exp_f32_e32 v206, v117
	v_exp_f32_e32 v207, v119
	s_nop 0
	v_cvt_pk_fp8_f32 v116, v204, v113
	v_cvt_pk_fp8_f32 v117, v205, v206
	v_cvt_pk_fp8_f32 v116, v114, v115 op_sel:[0,0,1]
	v_cvt_pk_fp8_f32 v117, v118, v207 op_sel:[0,0,1]
	s_waitcnt lgkmcnt(4)
	v_mfma_f32_32x32x64_f8f6f4 v[96:111], v[212:219], v[160:167], v[96:111]
	v_cvt_pk_fp8_f32 v112, v203, v220
	v_cvt_pk_fp8_f32 v113, v223, v224
	v_cvt_pk_fp8_f32 v114, v227, v228
	v_cvt_pk_fp8_f32 v118, v120, v121
	v_cvt_pk_fp8_f32 v115, v231, v232
	v_cvt_pk_fp8_f32 v119, v124, v125
	v_cvt_pk_fp8_f32 v112, v221, v222 op_sel:[0,0,1]
	v_cvt_pk_fp8_f32 v113, v225, v226 op_sel:[0,0,1]
	v_cvt_pk_fp8_f32 v114, v229, v230 op_sel:[0,0,1]
	v_cvt_pk_fp8_f32 v118, v122, v123 op_sel:[0,0,1]
	v_cvt_pk_fp8_f32 v115, v233, v234 op_sel:[0,0,1]
	v_cvt_pk_fp8_f32 v119, v126, v127 op_sel:[0,0,1]
	ds_read_b128 v[124:127], v200 offset:16384
	ds_read_b128 v[120:123], v199 offset:16384
	v_mfma_f32_32x32x64_f8f6f4 v[64:79], v[112:119], v[152:159], v[64:79]
	s_cmp_le_u32 s1, s39
	s_waitcnt lgkmcnt(4)
	v_mfma_f32_32x32x64_f8f6f4 v[48:63], v[112:119], v[236:243], v[48:63]
	ds_read_b128 v[236:239], v199 offset:18432
	ds_read_b128 v[240:243], v200 offset:18432
	s_waitcnt lgkmcnt(4)
	v_mfma_f32_32x32x64_f8f6f4 v[0:15], v[112:119], v[244:251], v[0:15]
	s_waitcnt lgkmcnt(2)
	v_mfma_f32_32x32x64_f8f6f4 v[32:47], v[112:119], v[120:127], v[32:47]
	s_waitcnt lgkmcnt(0)
	v_mfma_f32_32x32x64_f8f6f4 v[16:31], v[112:119], v[236:243], v[16:31]
	s_cbranch_scc1 .LBB0_603
; __device__ __forceinline__ void mask_tile(f32x16& p0, f32x16& p1, int dq, unsigned W) {
;     const float NEG = -__builtin_inff();
; #pragma unroll
;     for (int r = 0; r < 16; ++r) {
;         const int c = (r & 3) + 8 * (r >> 2);
;         if ((unsigned)(dq - c) >= W) p0[r] = NEG;
;         if ((unsigned)(dq - c - 32) >= W) p1[r] = NEG;
;     }
; }
	v_add_u32_e32 v112, 0x4000003b, v198
	v_cmp_gt_u32_e32 vcc, 2.0, v112
	v_add_u32_e32 v112, 27, v198
	s_nop 0
	v_cndmask_b32_e32 v128, v187, v128, vcc
	v_cmp_lt_u32_e32 vcc, s37, v112
	v_add_u32_e32 v112, 58, v198
	s_nop 0
	v_cndmask_b32_e32 v96, v187, v96, vcc
	v_cmp_lt_u32_e32 vcc, s37, v112
	v_add_u32_e32 v112, 26, v198
	s_nop 0
	v_cndmask_b32_e32 v129, v187, v129, vcc
	v_cmp_lt_u32_e32 vcc, s37, v112
	v_add_u32_e32 v112, 57, v198
	s_nop 0
	v_cndmask_b32_e32 v97, v187, v97, vcc
	v_cmp_lt_u32_e32 vcc, s37, v112
	v_add_u32_e32 v112, 25, v198
	s_nop 0
	v_cndmask_b32_e32 v130, v187, v130, vcc
	v_cmp_lt_u32_e32 vcc, s37, v112
	v_add_u32_e32 v112, 56, v198
	s_nop 0
	v_cndmask_b32_e32 v98, v187, v98, vcc
	v_cmp_lt_u32_e32 vcc, s37, v112
	v_add_u32_e32 v112, 24, v198
	s_nop 0
	v_cndmask_b32_e32 v131, v187, v131, vcc
	v_cmp_lt_u32_e32 vcc, s37, v112
	v_add_u32_e32 v112, 51, v198
	s_nop 0
	v_cndmask_b32_e32 v99, v187, v99, vcc
	v_cmp_lt_u32_e32 vcc, s37, v112
	v_add_u32_e32 v112, 19, v198
	s_nop 0
	v_cndmask_b32_e32 v132, v187, v132, vcc
	v_cmp_lt_u32_e32 vcc, s37, v112
	v_add_u32_e32 v112, 50, v198
	s_nop 0
	v_cndmask_b32_e32 v100, v187, v100, vcc
	v_cmp_lt_u32_e32 vcc, s37, v112
	v_add_u32_e32 v112, 18, v198
	s_nop 0
	v_cndmask_b32_e32 v133, v187, v133, vcc
	v_cmp_lt_u32_e32 vcc, s37, v112
	v_add_u32_e32 v112, 49, v198
	s_nop 0
	v_cndmask_b32_e32 v101, v187, v101, vcc
	v_cmp_lt_u32_e32 vcc, s37, v112
	v_add_u32_e32 v112, 17, v198
	s_nop 0
	v_cndmask_b32_e32 v134, v187, v134, vcc
	v_cmp_lt_u32_e32 vcc, s37, v112
	v_add_u32_e32 v112, 48, v198
	s_nop 0
	v_cndmask_b32_e32 v102, v187, v102, vcc
	v_cmp_lt_u32_e32 vcc, s37, v112
	v_add_u32_e32 v112, 16, v198
	s_nop 0
	v_cndmask_b32_e32 v135, v187, v135, vcc
	v_cmp_lt_u32_e32 vcc, s37, v112
	v_add_u32_e32 v112, 43, v198
	s_nop 0
	v_cndmask_b32_e32 v103, v187, v103, vcc
	v_cmp_lt_u32_e32 vcc, s37, v112
	v_add_u32_e32 v112, 11, v198
	s_nop 0
	v_cndmask_b32_e32 v136, v187, v136, vcc
	v_cmp_lt_u32_e32 vcc, s37, v112
	v_add_u32_e32 v112, 42, v198
	s_nop 0
	v_cndmask_b32_e32 v104, v187, v104, vcc
	v_cmp_lt_u32_e32 vcc, s37, v112
	v_add_u32_e32 v112, 10, v198
	s_nop 0
	v_cndmask_b32_e32 v137, v187, v137, vcc
	v_cmp_lt_u32_e32 vcc, s37, v112
	v_add_u32_e32 v112, 41, v198
	s_nop 0
	v_cndmask_b32_e32 v105, v187, v105, vcc
	v_cmp_lt_u32_e32 vcc, s37, v112
	v_add_u32_e32 v112, 9, v198
	s_nop 0
	v_cndmask_b32_e32 v138, v187, v138, vcc
	v_cmp_lt_u32_e32 vcc, s37, v112
	v_add_u32_e32 v112, 40, v198
	s_nop 0
	v_cndmask_b32_e32 v106, v187, v106, vcc
	v_cmp_lt_u32_e32 vcc, s37, v112
	v_add_u32_e32 v112, 8, v198
	s_nop 0
	v_cndmask_b32_e32 v139, v187, v139, vcc
	v_cmp_lt_u32_e32 vcc, s37, v112
	v_add_u32_e32 v112, 35, v198
	s_nop 0
	v_cndmask_b32_e32 v107, v187, v107, vcc
	v_cmp_lt_u32_e32 vcc, s37, v112
	v_add_u32_e32 v112, 3, v198
	s_nop 0
	v_cndmask_b32_e32 v140, v187, v140, vcc
	v_cmp_lt_u32_e32 vcc, s37, v112
	v_add_u32_e32 v112, 34, v198
	s_nop 0
	v_cndmask_b32_e32 v108, v187, v108, vcc
	v_cmp_lt_u32_e32 vcc, s37, v112
	v_add_u32_e32 v112, 2, v198
	s_nop 0
	v_cndmask_b32_e32 v141, v187, v141, vcc
	v_cmp_lt_u32_e32 vcc, s37, v112
	v_add_u32_e32 v112, 33, v198
	s_nop 0
	v_cndmask_b32_e32 v109, v187, v109, vcc
	v_cmp_lt_u32_e32 vcc, s37, v112
	v_add_u32_e32 v112, 1, v198
	s_nop 0
	v_cndmask_b32_e32 v142, v187, v142, vcc
	v_cmp_lt_u32_e32 vcc, s37, v112
	v_add_u32_e32 v112, 32, v198
	s_nop 0
	v_cndmask_b32_e32 v110, v187, v110, vcc
	v_cmp_lt_u32_e32 vcc, s37, v112
	s_nop 1
	v_cndmask_b32_e32 v143, v187, v143, vcc
	v_cmp_lt_u32_e32 vcc, s37, v198
	s_nop 1
	v_cndmask_b32_e32 v111, v187, v111, vcc

; __device__ __forceinline__ unsigned cvt_pk4_fp8(float a, float b, float c, float d) { int w; asm("" : "=v"(w));     w = __builtin_amdgcn_cvt_pk_fp8_f32(a, b, w, false); w = __builtin_amdgcn_cvt_pk_fp8_f32(c, d, w, true); return (unsigned)w; }
; __device__ __forceinline__ void finishSM(f32x16& p0, f32x16& p1, i32x8& pa) {
;     for (int r = 0; r < 16; ++r) p1[r] = __builtin_amdgcn_exp2f(p1[r]);
; #pragma unroll
;     for (int v = 0; v < 4; ++v) { pa[v] = (int)cvt_pk4_fp8(p0[4 * v], p0[4 * v + 1], p0[4 * v + 2], p0[4 * v + 3]); pa[4 + v] = (int)cvt_pk4_fp8(p1[4 * v], p1[4 * v + 1], p1[4 * v + 2], p1[4 * v + 3]); }
; }
; __device__ __forceinline__ void qkt(f32x16& p0, f32x16& p1, const char* stg, int ka, const i32x8* qf, const f32x16& minit) {
;     p0 = minit; p1 = minit;
; #pragma unroll
;     for (int s = 0; s < 3; ++s) { const char* a = stg + SOFF_K + s * 4096 + ka; const char* b = stg + SOFF_K + s * 4096 + (ka ^ 16);
;         const i32x4 a0 = *reinterpret_cast<const i32x4*>(a), a1 = *reinterpret_cast<const i32x4*>(b);
;         const i32x4 c0 = *reinterpret_cast<const i32x4*>(a + 2048), c1 = *reinterpret_cast<const i32x4*>(b + 2048);
;         p0 = __builtin_amdgcn_mfma_scale_f32_32x32x64_f8f6f4(__builtin_shufflevector(a0, a1, 0, 1, 2, 3, 4, 5, 6, 7), qf[s], p0, 0, 0, 0, 0, 0, 0);
;         p1 = __builtin_amdgcn_mfma_scale_f32_32x32x64_f8f6f4(__builtin_shufflevector(c0, c1, 0, 1, 2, 3, 4, 5, 6, 7), qf[s], p1, 0, 0, 0, 0, 0, 0); }
; }
; __device__ __forceinline__ void v_read(i32x8 (&vf)[4], const char* stg, int ka) {
; #pragma unroll
;     for (int d0 = 0; d0 < 4; ++d0) { const i32x4 a0 = *reinterpret_cast<const i32x4*>(stg + SOFF_V + d0 * 2048 + ka), a1 = *reinterpret_cast<const i32x4*>(stg + SOFF_V + d0 * 2048 + (ka ^ 16));
;         vf[d0] = __builtin_shufflevector(a0, a1, 0, 1, 2, 3, 4, 5, 6, 7); }
; }
; __device__ __forceinline__ void pv_mma(f32x16* o, f32x16& ol, const i32x8 (&vf)[4], const i32x8 ones, const i32x8 pa) {
; #pragma unroll
;     for (int d0 = 0; d0 < 4; ++d0) o[d0] = __builtin_amdgcn_mfma_scale_f32_32x32x64_f8f6f4(pa, vf[d0], o[d0], 0, 0, 0, 0, 0, 0);
;     ol = __builtin_amdgcn_mfma_scale_f32_32x32x64_f8f6f4(pa, ones, ol, 0, 0, 0, 0, 0, 0);
; }
.LBB0_674:
	s_cmp_gt_i32 s1, 3
	s_cselect_b32 s46, -4, 2
	s_add_i32 s1, s46, s1
	v_exp_f32_e32 v201, v128
	v_exp_f32_e32 v218, v129
	v_exp_f32_e32 v219, v130
	v_exp_f32_e32 v220, v131
	v_exp_f32_e32 v221, v132
	v_exp_f32_e32 v222, v133
	v_exp_f32_e32 v223, v134
	v_exp_f32_e32 v224, v135
	v_exp_f32_e32 v225, v136
	v_exp_f32_e32 v226, v137
	v_exp_f32_e32 v227, v138
	v_exp_f32_e32 v228, v139
	v_exp_f32_e32 v229, v140
	v_exp_f32_e32 v230, v141
	v_exp_f32_e32 v231, v142
	v_exp_f32_e32 v232, v143
	s_mul_i32 s92, s1, 0x5000
	s_add_i32 s46, s92, 0
	v_add_u32_e32 v233, s46, v193
	v_add_u32_e32 v234, s46, v194
	ds_read_b128 v[202:205], v233
	ds_read_b128 v[206:209], v234
	ds_read_b128 v[210:213], v233 offset:2048
	ds_read_b128 v[214:217], v234 offset:2048
	ds_read_b128 v[236:239], v233 offset:4096
	ds_read_b128 v[240:243], v234 offset:4096
	ds_read_b128 v[244:247], v233 offset:6144
	ds_read_b128 v[248:251], v234 offset:6144
	v_exp_f32_e32 v113, v113
	s_waitcnt lgkmcnt(6)
	v_mfma_f32_32x32x64_f8f6f4 v[128:143], v[202:209], v[168:175], v[80:95]
	v_exp_f32_e32 v114, v114
	v_exp_f32_e32 v115, v115
	v_exp_f32_e32 v118, v118
	v_exp_f32_e32 v120, v120
	v_exp_f32_e32 v121, v121
	v_exp_f32_e32 v124, v124
	v_exp_f32_e32 v125, v125
	v_exp_f32_e32 v122, v122
	v_exp_f32_e32 v123, v123
	v_exp_f32_e32 v126, v126
	v_exp_f32_e32 v127, v127
	s_waitcnt lgkmcnt(4)
	v_mfma_f32_32x32x64_f8f6f4 v[96:111], v[210:217], v[168:175], v[80:95]
	ds_read_b128 v[202:205], v233 offset:8192
	ds_read_b128 v[206:209], v234 offset:8192
	ds_read_b128 v[210:213], v233 offset:10240
	ds_read_b128 v[214:217], v234 offset:10240
	s_waitcnt lgkmcnt(6)
	v_mfma_f32_32x32x64_f8f6f4 v[128:143], v[236:243], v[176:183], v[128:143]
	s_waitcnt lgkmcnt(4)
	v_mfma_f32_32x32x64_f8f6f4 v[96:111], v[244:251], v[176:183], v[96:111]
	ds_read_b128 v[240:243], v200 offset:12288
	ds_read_b128 v[236:239], v199 offset:12288
	ds_read_b128 v[244:247], v199 offset:14336
	ds_read_b128 v[248:251], v200 offset:14336
	s_waitcnt lgkmcnt(6)
	v_mfma_f32_32x32x64_f8f6f4 v[128:143], v[202:209], v[160:167], v[128:143]
	v_exp_f32_e32 v202, v112
	v_exp_f32_e32 v203, v116
	v_exp_f32_e32 v204, v117
	v_exp_f32_e32 v205, v119
	s_nop 0
	v_cvt_pk_fp8_f32 v116, v202, v113
	v_cvt_pk_fp8_f32 v117, v203, v204
	v_cvt_pk_fp8_f32 v116, v114, v115 op_sel:[0,0,1]
	v_cvt_pk_fp8_f32 v117, v118, v205 op_sel:[0,0,1]
	s_waitcnt lgkmcnt(4)
	v_mfma_f32_32x32x64_f8f6f4 v[96:111], v[210:217], v[160:167], v[96:111]
	v_cvt_pk_fp8_f32 v112, v201, v218
	v_cvt_pk_fp8_f32 v113, v221, v222
	v_cvt_pk_fp8_f32 v114, v225, v226
	v_cvt_pk_fp8_f32 v118, v120, v121
	v_cvt_pk_fp8_f32 v115, v229, v230
	v_cvt_pk_fp8_f32 v119, v124, v125
	v_cvt_pk_fp8_f32 v112, v219, v220 op_sel:[0,0,1]
	v_cvt_pk_fp8_f32 v113, v223, v224 op_sel:[0,0,1]
	v_cvt_pk_fp8_f32 v114, v227, v228 op_sel:[0,0,1]
	v_cvt_pk_fp8_f32 v118, v122, v123 op_sel:[0,0,1]
	v_cvt_pk_fp8_f32 v115, v231, v232 op_sel:[0,0,1]
	v_cvt_pk_fp8_f32 v119, v126, v127 op_sel:[0,0,1]
	ds_read_b128 v[124:127], v200 offset:16384
	ds_read_b128 v[120:123], v199 offset:16384
	v_mfma_f32_32x32x64_f8f6f4 v[64:79], v[112:119], v[152:159], v[64:79]
	s_cmp_le_i32 s39, s0
	s_waitcnt lgkmcnt(4)
	v_mfma_f32_32x32x64_f8f6f4 v[48:63], v[112:119], v[236:243], v[48:63]
	ds_read_b128 v[236:239], v199 offset:18432
	ds_read_b128 v[240:243], v200 offset:18432
	s_waitcnt lgkmcnt(4)
	v_mfma_f32_32x32x64_f8f6f4 v[32:47], v[112:119], v[244:251], v[32:47]
	s_waitcnt lgkmcnt(2)
	v_mfma_f32_32x32x64_f8f6f4 v[16:31], v[112:119], v[120:127], v[16:31]
	s_waitcnt lgkmcnt(0)
	v_mfma_f32_32x32x64_f8f6f4 v[0:15], v[112:119], v[236:243], v[0:15]
	s_cbranch_scc1 .LBB0_676
; __device__ __forceinline__ void mask_tile(f32x16& p0, f32x16& p1, int dq, unsigned W) {
;     const float NEG = -__builtin_inff();
; #pragma unroll
;     for (int r = 0; r < 16; ++r) {
;         const int c = (r & 3) + 8 * (r >> 2);
;         if ((unsigned)(dq - c) >= W) p0[r] = NEG;
;         if ((unsigned)(dq - c - 32) >= W) p1[r] = NEG;
;     }
; }
	v_add_u32_e32 v112, 0x4000003b, v196
	v_cmp_gt_u32_e32 vcc, 2.0, v112
	v_add_u32_e32 v112, 27, v196
	s_nop 0
	v_cndmask_b32_e32 v128, v187, v128, vcc
	v_cmp_lt_u32_e32 vcc, s3, v112
	v_add_u32_e32 v112, 58, v196
	s_nop 0
	v_cndmask_b32_e32 v96, v187, v96, vcc
	v_cmp_lt_u32_e32 vcc, s3, v112
	v_add_u32_e32 v112, 26, v196
	s_nop 0
	v_cndmask_b32_e32 v129, v187, v129, vcc
	v_cmp_lt_u32_e32 vcc, s3, v112
	v_add_u32_e32 v112, 57, v196
	s_nop 0
	v_cndmask_b32_e32 v97, v187, v97, vcc
	v_cmp_lt_u32_e32 vcc, s3, v112
	v_add_u32_e32 v112, 25, v196
	s_nop 0
	v_cndmask_b32_e32 v130, v187, v130, vcc
	v_cmp_lt_u32_e32 vcc, s3, v112
	v_add_u32_e32 v112, 56, v196
	s_nop 0
	v_cndmask_b32_e32 v98, v187, v98, vcc
	v_cmp_lt_u32_e32 vcc, s3, v112
	v_add_u32_e32 v112, 24, v196
	s_nop 0
	v_cndmask_b32_e32 v131, v187, v131, vcc
	v_cmp_lt_u32_e32 vcc, s3, v112
	v_add_u32_e32 v112, 51, v196
	s_nop 0
	v_cndmask_b32_e32 v99, v187, v99, vcc
	v_cmp_lt_u32_e32 vcc, s3, v112
	v_add_u32_e32 v112, 19, v196
	s_nop 0
	v_cndmask_b32_e32 v132, v187, v132, vcc
	v_cmp_lt_u32_e32 vcc, s3, v112
	v_add_u32_e32 v112, 50, v196
	s_nop 0
	v_cndmask_b32_e32 v100, v187, v100, vcc
	v_cmp_lt_u32_e32 vcc, s3, v112
	v_add_u32_e32 v112, 18, v196
	s_nop 0
	v_cndmask_b32_e32 v133, v187, v133, vcc
	v_cmp_lt_u32_e32 vcc, s3, v112
	v_add_u32_e32 v112, 49, v196
	s_nop 0
	v_cndmask_b32_e32 v101, v187, v101, vcc
	v_cmp_lt_u32_e32 vcc, s3, v112
	v_add_u32_e32 v112, 17, v196
	s_nop 0
	v_cndmask_b32_e32 v134, v187, v134, vcc
	v_cmp_lt_u32_e32 vcc, s3, v112
	v_add_u32_e32 v112, 48, v196
	s_nop 0
	v_cndmask_b32_e32 v102, v187, v102, vcc
	v_cmp_lt_u32_e32 vcc, s3, v112
	v_add_u32_e32 v112, 16, v196
	s_nop 0
	v_cndmask_b32_e32 v135, v187, v135, vcc
	v_cmp_lt_u32_e32 vcc, s3, v112
	v_add_u32_e32 v112, 43, v196
	s_nop 0
	v_cndmask_b32_e32 v103, v187, v103, vcc
	v_cmp_lt_u32_e32 vcc, s3, v112
	v_add_u32_e32 v112, 11, v196
	s_nop 0
	v_cndmask_b32_e32 v136, v187, v136, vcc
	v_cmp_lt_u32_e32 vcc, s3, v112
	v_add_u32_e32 v112, 42, v196
	s_nop 0
	v_cndmask_b32_e32 v104, v187, v104, vcc
	v_cmp_lt_u32_e32 vcc, s3, v112
	v_add_u32_e32 v112, 10, v196
	s_nop 0
	v_cndmask_b32_e32 v137, v187, v137, vcc
	v_cmp_lt_u32_e32 vcc, s3, v112
	v_add_u32_e32 v112, 41, v196
	s_nop 0
	v_cndmask_b32_e32 v105, v187, v105, vcc
	v_cmp_lt_u32_e32 vcc, s3, v112
	v_add_u32_e32 v112, 9, v196
	s_nop 0
	v_cndmask_b32_e32 v138, v187, v138, vcc
	v_cmp_lt_u32_e32 vcc, s3, v112
	v_add_u32_e32 v112, 40, v196
	s_nop 0
	v_cndmask_b32_e32 v106, v187, v106, vcc
	v_cmp_lt_u32_e32 vcc, s3, v112
	v_add_u32_e32 v112, 8, v196
	s_nop 0
	v_cndmask_b32_e32 v139, v187, v139, vcc
	v_cmp_lt_u32_e32 vcc, s3, v112
	v_add_u32_e32 v112, 35, v196
	s_nop 0
	v_cndmask_b32_e32 v107, v187, v107, vcc
	v_cmp_lt_u32_e32 vcc, s3, v112
	v_add_u32_e32 v112, 3, v196
	s_nop 0
	v_cndmask_b32_e32 v140, v187, v140, vcc
	v_cmp_lt_u32_e32 vcc, s3, v112
	v_add_u32_e32 v112, 34, v196
	s_nop 0
	v_cndmask_b32_e32 v108, v187, v108, vcc
	v_cmp_lt_u32_e32 vcc, s3, v112
	v_add_u32_e32 v112, 2, v196
	s_nop 0
	v_cndmask_b32_e32 v141, v187, v141, vcc
	v_cmp_lt_u32_e32 vcc, s3, v112
	v_add_u32_e32 v112, 33, v196
	s_nop 0
	v_cndmask_b32_e32 v109, v187, v109, vcc
	v_cmp_lt_u32_e32 vcc, s3, v112
	v_add_u32_e32 v112, 1, v196
	s_nop 0
	v_cndmask_b32_e32 v142, v187, v142, vcc
	v_cmp_lt_u32_e32 vcc, s3, v112
	v_add_u32_e32 v112, 32, v196
	s_nop 0
	v_cndmask_b32_e32 v110, v187, v110, vcc
	v_cmp_lt_u32_e32 vcc, s3, v112
	s_nop 1
	v_cndmask_b32_e32 v143, v187, v143, vcc
	v_cmp_lt_u32_e32 vcc, s3, v196
	s_nop 1
	v_cndmask_b32_e32 v111, v187, v111, vcc

; __device__ __forceinline__ unsigned cvt_pk4_fp8(float a, float b, float c, float d) { int w; asm("" : "=v"(w));     w = __builtin_amdgcn_cvt_pk_fp8_f32(a, b, w, false); w = __builtin_amdgcn_cvt_pk_fp8_f32(c, d, w, true); return (unsigned)w; }
; __device__ __forceinline__ void finishSM(f32x16& p0, f32x16& p1, i32x8& pa) {
;     for (int r = 0; r < 16; ++r) p1[r] = __builtin_amdgcn_exp2f(p1[r]);
; #pragma unroll
;     for (int v = 0; v < 4; ++v) { pa[v] = (int)cvt_pk4_fp8(p0[4 * v], p0[4 * v + 1], p0[4 * v + 2], p0[4 * v + 3]); pa[4 + v] = (int)cvt_pk4_fp8(p1[4 * v], p1[4 * v + 1], p1[4 * v + 2], p1[4 * v + 3]); }
; }
; __device__ __forceinline__ void qkt(f32x16& p0, f32x16& p1, const char* stg, int ka, const i32x8* qf, const f32x16& minit) {
;     p0 = minit; p1 = minit;
; #pragma unroll
;     for (int s = 0; s < 3; ++s) { const char* a = stg + SOFF_K + s * 4096 + ka; const char* b = stg + SOFF_K + s * 4096 + (ka ^ 16);
;         const i32x4 a0 = *reinterpret_cast<const i32x4*>(a), a1 = *reinterpret_cast<const i32x4*>(b);
;         const i32x4 c0 = *reinterpret_cast<const i32x4*>(a + 2048), c1 = *reinterpret_cast<const i32x4*>(b + 2048);
;         p0 = __builtin_amdgcn_mfma_scale_f32_32x32x64_f8f6f4(__builtin_shufflevector(a0, a1, 0, 1, 2, 3, 4, 5, 6, 7), qf[s], p0, 0, 0, 0, 0, 0, 0);
;         p1 = __builtin_amdgcn_mfma_scale_f32_32x32x64_f8f6f4(__builtin_shufflevector(c0, c1, 0, 1, 2, 3, 4, 5, 6, 7), qf[s], p1, 0, 0, 0, 0, 0, 0); }
; }
; __device__ __forceinline__ void v_read(i32x8 (&vf)[4], const char* stg, int ka) {
; #pragma unroll
;     for (int d0 = 0; d0 < 4; ++d0) { const i32x4 a0 = *reinterpret_cast<const i32x4*>(stg + SOFF_V + d0 * 2048 + ka), a1 = *reinterpret_cast<const i32x4*>(stg + SOFF_V + d0 * 2048 + (ka ^ 16));
;         vf[d0] = __builtin_shufflevector(a0, a1, 0, 1, 2, 3, 4, 5, 6, 7); }
; }
; __device__ __forceinline__ void pv_mma(f32x16* o, f32x16& ol, const i32x8 (&vf)[4], const i32x8 ones, const i32x8 pa) {
; #pragma unroll
;     for (int d0 = 0; d0 < 4; ++d0) o[d0] = __builtin_amdgcn_mfma_scale_f32_32x32x64_f8f6f4(pa, vf[d0], o[d0], 0, 0, 0, 0, 0, 0);
;     ol = __builtin_amdgcn_mfma_scale_f32_32x32x64_f8f6f4(pa, ones, ol, 0, 0, 0, 0, 0, 0);
; }
.LBB0_736:
	s_cmp_gt_i32 s0, 3
	s_cselect_b32 s36, -4, 2
	s_add_i32 s0, s36, s0
	v_exp_f32_e32 v203, v128
	v_exp_f32_e32 v220, v129
	v_exp_f32_e32 v221, v130
	v_exp_f32_e32 v222, v131
	v_exp_f32_e32 v223, v132
	v_exp_f32_e32 v224, v133
	v_exp_f32_e32 v225, v134
	v_exp_f32_e32 v226, v135
	v_exp_f32_e32 v227, v136
	v_exp_f32_e32 v228, v137
	v_exp_f32_e32 v229, v138
	v_exp_f32_e32 v230, v139
	v_exp_f32_e32 v231, v140
	v_exp_f32_e32 v232, v141
	v_exp_f32_e32 v233, v142
	v_exp_f32_e32 v234, v143
	s_mul_i32 s36, s0, 0x5000
	s_add_i32 s36, s36, 0
	v_add_u32_e32 v202, s36, v192
	v_add_u32_e32 v201, s36, v193
	ds_read_b128 v[204:207], v202
	ds_read_b128 v[208:211], v201
	ds_read_b128 v[212:215], v202 offset:2048
	ds_read_b128 v[216:219], v201 offset:2048
	ds_read_b128 v[236:239], v202 offset:4096
	ds_read_b128 v[240:243], v201 offset:4096
	ds_read_b128 v[244:247], v202 offset:6144
	ds_read_b128 v[248:251], v201 offset:6144
	v_exp_f32_e32 v113, v113
	s_waitcnt lgkmcnt(6)
	v_mfma_f32_32x32x64_f8f6f4 v[128:143], v[204:211], v[168:175], v[80:95]
	v_exp_f32_e32 v114, v114
	v_exp_f32_e32 v115, v115
	v_exp_f32_e32 v118, v118
	v_exp_f32_e32 v120, v120
	v_exp_f32_e32 v121, v121
	v_exp_f32_e32 v124, v124
	v_exp_f32_e32 v125, v125
	v_exp_f32_e32 v122, v122
	v_exp_f32_e32 v123, v123
	v_exp_f32_e32 v126, v126
	v_exp_f32_e32 v127, v127
	s_waitcnt lgkmcnt(4)
	v_mfma_f32_32x32x64_f8f6f4 v[96:111], v[212:219], v[168:175], v[80:95]
	ds_read_b128 v[204:207], v202 offset:8192
	ds_read_b128 v[208:211], v201 offset:8192
	ds_read_b128 v[212:215], v202 offset:10240
	ds_read_b128 v[216:219], v201 offset:10240
	s_waitcnt lgkmcnt(6)
	v_mfma_f32_32x32x64_f8f6f4 v[128:143], v[236:243], v[176:183], v[128:143]
	s_waitcnt lgkmcnt(4)
	v_mfma_f32_32x32x64_f8f6f4 v[96:111], v[244:251], v[176:183], v[96:111]
	ds_read_b128 v[240:243], v200 offset:12288
	ds_read_b128 v[236:239], v199 offset:12288
	ds_read_b128 v[244:247], v199 offset:14336
	ds_read_b128 v[248:251], v200 offset:14336
	s_waitcnt lgkmcnt(6)
	v_mfma_f32_32x32x64_f8f6f4 v[128:143], v[204:211], v[160:167], v[128:143]
	v_exp_f32_e32 v204, v112
	v_exp_f32_e32 v205, v116
	v_exp_f32_e32 v206, v117
	v_exp_f32_e32 v207, v119
	s_nop 0
	v_cvt_pk_fp8_f32 v116, v204, v113
	v_cvt_pk_fp8_f32 v117, v205, v206
	v_cvt_pk_fp8_f32 v116, v114, v115 op_sel:[0,0,1]
	v_cvt_pk_fp8_f32 v117, v118, v207 op_sel:[0,0,1]
	s_waitcnt lgkmcnt(4)
	v_mfma_f32_32x32x64_f8f6f4 v[96:111], v[212:219], v[160:167], v[96:111]
	v_cvt_pk_fp8_f32 v112, v203, v220
	v_cvt_pk_fp8_f32 v113, v223, v224
	v_cvt_pk_fp8_f32 v114, v227, v228
	v_cvt_pk_fp8_f32 v118, v120, v121
	v_cvt_pk_fp8_f32 v115, v231, v232
	v_cvt_pk_fp8_f32 v119, v124, v125
	v_cvt_pk_fp8_f32 v112, v221, v222 op_sel:[0,0,1]
	v_cvt_pk_fp8_f32 v113, v225, v226 op_sel:[0,0,1]
	v_cvt_pk_fp8_f32 v114, v229, v230 op_sel:[0,0,1]
	v_cvt_pk_fp8_f32 v118, v122, v123 op_sel:[0,0,1]
	v_cvt_pk_fp8_f32 v115, v233, v234 op_sel:[0,0,1]
	v_cvt_pk_fp8_f32 v119, v126, v127 op_sel:[0,0,1]
	ds_read_b128 v[124:127], v200 offset:16384
	ds_read_b128 v[120:123], v199 offset:16384
	v_mfma_f32_32x32x64_f8f6f4 v[64:79], v[112:119], v[152:159], v[64:79]
	s_cmp_le_u32 s1, s39
	s_waitcnt lgkmcnt(4)
	v_mfma_f32_32x32x64_f8f6f4 v[48:63], v[112:119], v[236:243], v[48:63]
	ds_read_b128 v[236:239], v199 offset:18432
	ds_read_b128 v[240:243], v200 offset:18432
	s_waitcnt lgkmcnt(4)
	v_mfma_f32_32x32x64_f8f6f4 v[0:15], v[112:119], v[244:251], v[0:15]
	s_waitcnt lgkmcnt(2)
	v_mfma_f32_32x32x64_f8f6f4 v[32:47], v[112:119], v[120:127], v[32:47]
	s_waitcnt lgkmcnt(0)
	v_mfma_f32_32x32x64_f8f6f4 v[16:31], v[112:119], v[236:243], v[16:31]
	s_cbranch_scc1 .LBB0_738
; __device__ __forceinline__ void mask_tile(f32x16& p0, f32x16& p1, int dq, unsigned W) {
;     const float NEG = -__builtin_inff();
; #pragma unroll
;     for (int r = 0; r < 16; ++r) {
;         const int c = (r & 3) + 8 * (r >> 2);
;         if ((unsigned)(dq - c) >= W) p0[r] = NEG;
;         if ((unsigned)(dq - c - 32) >= W) p1[r] = NEG;
;     }
; }
	v_add_u32_e32 v112, 0x4000003b, v198
	v_cmp_gt_u32_e32 vcc, 2.0, v112
	v_add_u32_e32 v112, 27, v198
	s_nop 0
	v_cndmask_b32_e32 v128, v187, v128, vcc
	v_cmp_lt_u32_e32 vcc, s41, v112
	v_add_u32_e32 v112, 58, v198
	s_nop 0
	v_cndmask_b32_e32 v96, v187, v96, vcc
	v_cmp_lt_u32_e32 vcc, s41, v112
	v_add_u32_e32 v112, 26, v198
	s_nop 0
	v_cndmask_b32_e32 v129, v187, v129, vcc
	v_cmp_lt_u32_e32 vcc, s41, v112
	v_add_u32_e32 v112, 57, v198
	s_nop 0
	v_cndmask_b32_e32 v97, v187, v97, vcc
	v_cmp_lt_u32_e32 vcc, s41, v112
	v_add_u32_e32 v112, 25, v198
	s_nop 0
	v_cndmask_b32_e32 v130, v187, v130, vcc
	v_cmp_lt_u32_e32 vcc, s41, v112
	v_add_u32_e32 v112, 56, v198
	s_nop 0
	v_cndmask_b32_e32 v98, v187, v98, vcc
	v_cmp_lt_u32_e32 vcc, s41, v112
	v_add_u32_e32 v112, 24, v198
	s_nop 0
	v_cndmask_b32_e32 v131, v187, v131, vcc
	v_cmp_lt_u32_e32 vcc, s41, v112
	v_add_u32_e32 v112, 51, v198
	s_nop 0
	v_cndmask_b32_e32 v99, v187, v99, vcc
	v_cmp_lt_u32_e32 vcc, s41, v112
	v_add_u32_e32 v112, 19, v198
	s_nop 0
	v_cndmask_b32_e32 v132, v187, v132, vcc
	v_cmp_lt_u32_e32 vcc, s41, v112
	v_add_u32_e32 v112, 50, v198
	s_nop 0
	v_cndmask_b32_e32 v100, v187, v100, vcc
	v_cmp_lt_u32_e32 vcc, s41, v112
	v_add_u32_e32 v112, 18, v198
	s_nop 0
	v_cndmask_b32_e32 v133, v187, v133, vcc
	v_cmp_lt_u32_e32 vcc, s41, v112
	v_add_u32_e32 v112, 49, v198
	s_nop 0
	v_cndmask_b32_e32 v101, v187, v101, vcc
	v_cmp_lt_u32_e32 vcc, s41, v112
	v_add_u32_e32 v112, 17, v198
	s_nop 0
	v_cndmask_b32_e32 v134, v187, v134, vcc
	v_cmp_lt_u32_e32 vcc, s41, v112
	v_add_u32_e32 v112, 48, v198
	s_nop 0
	v_cndmask_b32_e32 v102, v187, v102, vcc
	v_cmp_lt_u32_e32 vcc, s41, v112
	v_add_u32_e32 v112, 16, v198
	s_nop 0
	v_cndmask_b32_e32 v135, v187, v135, vcc
	v_cmp_lt_u32_e32 vcc, s41, v112
	v_add_u32_e32 v112, 43, v198
	s_nop 0
	v_cndmask_b32_e32 v103, v187, v103, vcc
	v_cmp_lt_u32_e32 vcc, s41, v112
	v_add_u32_e32 v112, 11, v198
	s_nop 0
	v_cndmask_b32_e32 v136, v187, v136, vcc
	v_cmp_lt_u32_e32 vcc, s41, v112
	v_add_u32_e32 v112, 42, v198
	s_nop 0
	v_cndmask_b32_e32 v104, v187, v104, vcc
	v_cmp_lt_u32_e32 vcc, s41, v112
	v_add_u32_e32 v112, 10, v198
	s_nop 0
	v_cndmask_b32_e32 v137, v187, v137, vcc
	v_cmp_lt_u32_e32 vcc, s41, v112
	v_add_u32_e32 v112, 41, v198
	s_nop 0
	v_cndmask_b32_e32 v105, v187, v105, vcc
	v_cmp_lt_u32_e32 vcc, s41, v112
	v_add_u32_e32 v112, 9, v198
	s_nop 0
	v_cndmask_b32_e32 v138, v187, v138, vcc
	v_cmp_lt_u32_e32 vcc, s41, v112
	v_add_u32_e32 v112, 40, v198
	s_nop 0
	v_cndmask_b32_e32 v106, v187, v106, vcc
	v_cmp_lt_u32_e32 vcc, s41, v112
	v_add_u32_e32 v112, 8, v198
	s_nop 0
	v_cndmask_b32_e32 v139, v187, v139, vcc
	v_cmp_lt_u32_e32 vcc, s41, v112
	v_add_u32_e32 v112, 35, v198
	s_nop 0
	v_cndmask_b32_e32 v107, v187, v107, vcc
	v_cmp_lt_u32_e32 vcc, s41, v112
	v_add_u32_e32 v112, 3, v198
	s_nop 0
	v_cndmask_b32_e32 v140, v187, v140, vcc
	v_cmp_lt_u32_e32 vcc, s41, v112
	v_add_u32_e32 v112, 34, v198
	s_nop 0
	v_cndmask_b32_e32 v108, v187, v108, vcc
	v_cmp_lt_u32_e32 vcc, s41, v112
	v_add_u32_e32 v112, 2, v198
	s_nop 0
	v_cndmask_b32_e32 v141, v187, v141, vcc
	v_cmp_lt_u32_e32 vcc, s41, v112
	v_add_u32_e32 v112, 33, v198
	s_nop 0
	v_cndmask_b32_e32 v109, v187, v109, vcc
	v_cmp_lt_u32_e32 vcc, s41, v112
	v_add_u32_e32 v112, 1, v198
	s_nop 0
	v_cndmask_b32_e32 v142, v187, v142, vcc
	v_cmp_lt_u32_e32 vcc, s41, v112
	v_add_u32_e32 v112, 32, v198
	s_nop 0
	v_cndmask_b32_e32 v110, v187, v110, vcc
	v_cmp_lt_u32_e32 vcc, s41, v112
	s_nop 1
	v_cndmask_b32_e32 v143, v187, v143, vcc
	v_cmp_lt_u32_e32 vcc, s41, v198
	s_nop 1
	v_cndmask_b32_e32 v111, v187, v111, vcc
